# K/V-loader-wave conversion with fewer branches / scalar ops per piece (kind selected with s_cselect, two-variant waits)
# speedup vs baseline: 1.0130x; 1.0025x over previous
.LBB0_1198:
	s_cmp_ge_i32 s53, s35
	s_cbranch_scc1 .LBB0_1428
	s_load_dwordx2 s[14:15], s[10:11], 0xd8
	v_mov_b32_e32 v1, 0x3fb8aa3b
	v_mul_f32_e32 v3, s7, v1
	v_mul_f32_e32 v1, s3, v1
	v_mul_f32_e32 v2, 0x4f7ffffe, v2
	s_waitcnt lgkmcnt(0)
	s_add_u32 s3, s14, 0x25b00000
	s_addc_u32 s8, s15, 0
	s_add_u32 s16, s14, 0x29c00000
	s_addc_u32 s17, s15, 0
	s_add_u32 s9, s14, 0x3a000000
	s_addc_u32 s26, s15, 0
	v_cvt_u32_f32_e32 v2, v2
	s_add_u32 s27, s14, 0x31e00000
	s_addc_u32 s23, s15, 0
	v_writelane_b32 v255, s20, 8
	s_and_b64 s[18:19], s[12:13], exec
	s_cselect_b32 s18, s6, s22
	v_writelane_b32 v255, s21, 9
	s_sub_i32 s21, 0, s6
	v_readfirstlane_b32 s28, v2
	s_mul_i32 s21, s21, s28
	s_mul_hi_u32 s21, s28, s21
	s_abs_i32 s20, s88
	s_add_i32 s28, s28, s21
	s_mul_hi_u32 s21, s20, s28
	s_mul_i32 s28, s21, s6
	v_readlane_b32 s7, v255, 6
	s_sub_i32 s20, s20, s28
	s_lshl_b32 s19, s7, 5
	s_ashr_i32 s7, s88, 31
	s_add_i32 s28, s21, 1
	s_sub_i32 s29, s20, s6
	s_cmp_ge_u32 s20, s6
	v_exp_f32_e32 v3, v3
	v_exp_f32_e32 v1, v1
	s_cselect_b32 s21, s28, s21
	s_cselect_b32 s20, s29, s20
	s_add_i32 s28, s21, 1
	s_cmp_ge_u32 s20, s6
	s_cselect_b32 s6, s28, s21
	v_sub_f32_e32 v1, v3, v1
	v_lshl_add_u32 v3, v0, 2, 0
	s_xor_b32 s6, s6, s7
	v_cndmask_b32_e64 v2, 0, 1, s[4:5]
	v_add_f32_e32 v1, 0x3eb60549, v1
	s_mov_b32 s36, 0
	v_add_u32_e32 v179, 0xc800, v3
	s_sub_i32 s20, s6, s7
	v_cmp_ne_u32_e64 s[4:5], 1, v2
	s_movk_i32 s21, 0xffc0
	v_mov_b32_e32 v181, 0
	s_mov_b32 s54, 0x41000000
	s_mov_b64 s[56:57], 0x3a004000
	s_mov_b64 s[58:59], 0x3a005000
	s_mov_b64 s[60:61], 0x3a006000
	s_mov_b64 s[62:63], 0x3a007000
	s_mov_b64 s[64:65], 0x3a008000
	s_mov_b64 s[66:67], 0x3a009000
	s_mov_b64 s[68:69], 0x3a00a000
	s_mov_b64 s[70:71], 0x3a00b000
	s_mov_b64 s[72:73], 0x8000
	s_mov_b64 s[74:75], 0x40000
	s_mov_b64 s[82:83], 0x206000
	s_mov_b64 s[84:85], 0x207000
	s_load_dwordx2 s[100:101], s[0:1], 0xb0
	s_waitcnt lgkmcnt(0)
	s_add_u32 s100, s100, 0x10000000
	s_addc_u32 s101, s101, 0
	v_writelane_b32 v254, s100, 0
	v_writelane_b32 v254, s101, 1
	s_load_dwordx2 s[100:101], s[0:1], 0xc0
	s_waitcnt lgkmcnt(0)
	s_sub_u32 s100, s100, 0x8000000
	s_subb_u32 s101, s101, 0
	v_writelane_b32 v254, s100, 2
	v_writelane_b32 v254, s101, 3
	s_load_dwordx2 s[100:101], s[0:1], 0xd8
	s_waitcnt lgkmcnt(0)
	v_writelane_b32 v254, s100, 4
	v_writelane_b32 v254, s101, 5
	v_readfirstlane_b32 s100, v0
	s_lshr_b32 s100, s100, 6
	s_lshl_b32 s101, s2, 2
	s_add_i32 s100, s100, s101
	s_lshr_b32 s101, s100, 5
	s_lshl_b32 s101, s101, 15
	s_and_b32 s98, s100, 31
	s_lshl_b32 s98, s98, 8
	s_add_i32 s101, s101, s98
	v_writelane_b32 v254, s101, 6
	s_and_b32 s98, s100, 15
	s_lshr_b32 s98, s98, 1
	s_lshl_b32 s98, s98, 8
	s_bfe_u32 s99, s100, 0x10004
	s_lshl_b32 s99, s99, 7
	s_add_i32 s98, s98, s99
	s_and_b32 s99, s100, 1
	s_lshl_b32 s99, s99, 6
	s_add_i32 s98, s98, s99
	s_lshl_b32 s98, s98, 10
	s_lshr_b32 s99, s100, 5
	s_lshl_b32 s99, s99, 2
	s_add_i32 s98, s98, s99
	s_add_i32 s98, s98, 0x5800000
	v_writelane_b32 v254, s98, 7
	s_lshr_b32 s98, s100, 4
	s_lshl_b32 s99, s98, 14
	s_and_b32 s101, s100, 15
	s_lshl_b32 s101, s101, 8
	s_add_i32 s99, s99, s101
	v_writelane_b32 v254, s99, 8
	s_lshl_b32 s99, s98, 2
	s_and_b32 s101, s100, 15
	s_lshl_b32 s101, s101, 16
	s_add_i32 s99, s99, s101
	s_add_i32 s99, s99, 0x13800000
	v_writelane_b32 v254, s99, 9
	v_and_b32_e32 v240, 63, v0
	v_lshrrev_b32_e32 v252, 4, v240
	v_and_b32_e32 v253, 15, v240
	v_lshlrev_b32_e32 v243, 4, v253
	v_lshl_add_u32 v253, v253, 2, v252
	v_lshlrev_b32_e32 v253, 10, v253
	v_mov_b32_e32 v240, v243
	s_cmpk_eq_u32 s22, 0x100
	s_cselect_b32 s32, 0, 0x180
	s_mov_b32 s98, 0
	s_mov_b32 s99, 0
	v_mov_b32_e32 v184, 0x3727c5ac
	s_mov_b32 s55, 0xf800000
	v_mov_b32_e32 v185, 0x260
	s_branch .LBB0_1203

.LBB0_1268:
	s_add_i32 s49, s45, 0x3000
	v_lshl_add_u64 v[130:131], s[14:15], 0, v[174:175]
	s_mov_b32 m0, s49
	v_lshl_add_u64 v[176:177], s[14:15], 0, v[172:173]
	s_add_i32 s47, s46, 0x8000
	global_load_lds_dwordx4 v[130:131], off
	v_lshl_add_u64 v[130:131], v[176:177], 0, s[56:57]
	s_mov_b32 m0, s47
	s_add_i32 s48, s46, 0x9000
	global_load_lds_dwordx4 v[130:131], off
	v_lshl_add_u64 v[130:131], v[176:177], 0, s[58:59]
	s_mov_b32 m0, s48
	v_cvt_pk_fp8_f32 v162, v114, v115
	global_load_lds_dwordx4 v[130:131], off
	s_and_b32 s100, s32, 0x3ff
	s_cmpk_lt_u32 s100, 0x180
	s_cbranch_scc0 .Lkc_i9_r0
	s_cmpk_lt_u32 s100, 0x100
	s_cselect_b32 vcc_lo, 6, 8
	s_cselect_b32 vcc_hi, 13, 12
	s_lshl_b32 s100, s100, 20
	v_readlane_b32 s101, v254, vcc_lo
	s_add_i32 s100, s100, s101
	v_lshl_add_u32 v238, v252, vcc_hi, v240
	v_add_u32_e32 v238, s100, v238
	s_sub_i32 vcc_lo, vcc_lo, 6
	v_readlane_b32 s100, v254, vcc_lo
	s_add_i32 vcc_lo, vcc_lo, 1
	v_readlane_b32 s101, v254, vcc_lo
	v_mov_b32_e32 v239, 0
	s_nop 1
	v_lshl_add_u64 v[238:239], v[238:239], 0, s[100:101]
	global_load_dwordx4 v[234:237], v[238:239], off
	s_or_b32 s32, s32, 0xc0000000

.LBB0_1275:
	s_add_i32 s38, s88, s37
	s_cmpk_eq_i32 s44, 0xf9
	s_cselect_b32 s38, s77, s38
	s_ashr_i32 s39, s38, 31
	s_lshl_b64 s[38:39], s[38:39], 10
	s_mov_b32 m0, s45
	s_lshr_b32 s100, s32, 29
	s_and_b32 s100, s100, 5
	s_cmp_eq_u32 s100, 5
	s_cbranch_scc1 .Lkc_w05_r0
	s_waitcnt vmcnt(3) lgkmcnt(0)
	s_branch .Lkc_w0e_r0
